# baseline (speedup 1.0000x reference)
.Lk2_b00:
	s_waitcnt lgkmcnt(4)
	v_mfma_f32_32x32x16_f16 v[16:31], v[144:147], v[80:83], v[16:31]
	v_mfma_f32_32x32x16_f16 v[0:15], v[144:147], v[84:87], v[0:15]
	v_mfma_f32_32x32x16_f16 v[16:31], v[148:151], v[88:91], v[16:31]
	v_mfma_f32_32x32x16_f16 v[0:15], v[148:151], v[92:95], v[0:15]
	s_cmp_le_u32 s22, 16
	s_cselect_b32 s40, s18, 0x18000
	s_add_u32 m0, s40, s35
	s_add_u32 s22, s22, 1
	global_load_lds_dwordx4 v168, s[20:21]
	global_load_lds_dwordx4 v168, s[20:21] offset:1024
	v_pk_mul_f16 v152, v48, v32 op_sel:[1,0] op_sel_hi:[1,1]
	v_pk_mul_f16 v153, v48, v33 op_sel:[1,0] op_sel_hi:[1,1]
	v_pk_mul_f16 v154, v48, v34 op_sel:[1,0] op_sel_hi:[1,1]
	v_pk_mul_f16 v155, v48, v35 op_sel:[1,0] op_sel_hi:[1,1]
	s_cmp_le_u32 s22, 16
	s_cselect_b32 s41, 0x4000, 0
	v_pk_fma_f16 v152, v40, v36, v152 op_sel:[1,0,0] op_sel_hi:[1,1,1]
	v_pk_fma_f16 v153, v40, v37, v153 op_sel:[1,0,0] op_sel_hi:[1,1,1]
	v_pk_fma_f16 v154, v40, v38, v154 op_sel:[1,0,0] op_sel_hi:[1,1,1]
	v_pk_fma_f16 v155, v40, v39, v155 op_sel:[1,0,0] op_sel_hi:[1,1,1]
	s_add_u32 s20, s20, s41
	s_addc_u32 s21, s21, 0
	v_pk_mul_f16 v156, v48, v36 op_sel:[1,0] op_sel_hi:[1,1]
	v_pk_mul_f16 v157, v48, v37 op_sel:[1,0] op_sel_hi:[1,1]
	v_pk_mul_f16 v158, v48, v38 op_sel:[1,0] op_sel_hi:[1,1]
	v_pk_mul_f16 v159, v48, v39 op_sel:[1,0] op_sel_hi:[1,1]
	s_add_u32 s18, s18, 0x4000
	s_cmp_eq_u32 s18, 0x18000
	s_cselect_b32 s18, 0, s18
	v_pk_fma_f16 v156, v40, v32, v156 op_sel:[1,0,0] op_sel_hi:[1,1,1] neg_lo:[0,0,1] neg_hi:[0,0,1]
	v_pk_fma_f16 v157, v40, v33, v157 op_sel:[1,0,0] op_sel_hi:[1,1,1] neg_lo:[0,0,1] neg_hi:[0,0,1]
	v_pk_fma_f16 v158, v40, v34, v158 op_sel:[1,0,0] op_sel_hi:[1,1,1] neg_lo:[0,0,1] neg_hi:[0,0,1]
	v_pk_fma_f16 v159, v40, v35, v159 op_sel:[1,0,0] op_sel_hi:[1,1,1] neg_lo:[0,0,1] neg_hi:[0,0,1]
	ds_read_b128 v[112:115], v161 offset:8192
	ds_read_b128 v[116:119], v161 offset:9216
	ds_read_b128 v[120:123], v161 offset:10240
	ds_read_b128 v[124:127], v161 offset:11264
	s_waitcnt lgkmcnt(4)
	v_mfma_f32_32x32x16_f16 v[16:31], v[152:155], v[96:99], v[16:31]
	v_mfma_f32_32x32x16_f16 v[0:15], v[152:155], v[100:103], v[0:15]
	v_mfma_f32_32x32x16_f16 v[16:31], v[156:159], v[104:107], v[16:31]
	v_mfma_f32_32x32x16_f16 v[0:15], v[156:159], v[108:111], v[0:15]
	s_add_u32 s14, s14, 1
	s_cmp_eq_u32 s14, 16
	s_cselect_b32 s42, 1, 0
	v_pk_mul_f16 v144, v49, v32 op_sel:[0,0] op_sel_hi:[0,1]
	v_pk_mul_f16 v145, v49, v33 op_sel:[0,0] op_sel_hi:[0,1]
	v_pk_mul_f16 v146, v49, v34 op_sel:[0,0] op_sel_hi:[0,1]
	v_pk_mul_f16 v147, v49, v35 op_sel:[0,0] op_sel_hi:[0,1]
	s_add_u32 s13, s13, s42
	s_cmp_eq_u32 s42, 1
	s_cselect_b32 s14, s13, s14
	v_pk_fma_f16 v144, v41, v36, v144 op_sel:[0,0,0] op_sel_hi:[0,1,1]
	v_pk_fma_f16 v145, v41, v37, v145 op_sel:[0,0,0] op_sel_hi:[0,1,1]
	v_pk_fma_f16 v146, v41, v38, v146 op_sel:[0,0,0] op_sel_hi:[0,1,1]
	v_pk_fma_f16 v147, v41, v39, v147 op_sel:[0,0,0] op_sel_hi:[0,1,1]
	s_min_u32 s43, s13, 15
	s_min_u32 s44, s14, 15
	s_lshl_b32 s45, s44, 16
	v_pk_mul_f16 v148, v49, v36 op_sel:[0,0] op_sel_hi:[0,1]
	v_pk_mul_f16 v149, v49, v37 op_sel:[0,0] op_sel_hi:[0,1]
	v_pk_mul_f16 v150, v49, v38 op_sel:[0,0] op_sel_hi:[0,1]
	v_pk_mul_f16 v151, v49, v39 op_sel:[0,0] op_sel_hi:[0,1]
	s_add_u32 s24, s8, s45
	s_addc_u32 s25, s9, 0
	v_pk_fma_f16 v148, v41, v32, v148 op_sel:[0,0,0] op_sel_hi:[0,1,1] neg_lo:[0,0,1] neg_hi:[0,0,1]
	v_pk_fma_f16 v149, v41, v33, v149 op_sel:[0,0,0] op_sel_hi:[0,1,1] neg_lo:[0,0,1] neg_hi:[0,0,1]
	v_pk_fma_f16 v150, v41, v34, v150 op_sel:[0,0,0] op_sel_hi:[0,1,1] neg_lo:[0,0,1] neg_hi:[0,0,1]
	v_pk_fma_f16 v151, v41, v35, v151 op_sel:[0,0,0] op_sel_hi:[0,1,1] neg_lo:[0,0,1] neg_hi:[0,0,1]
	ds_read_b128 v[128:131], v161 offset:12288
	ds_read_b128 v[132:135], v161 offset:13312
	ds_read_b128 v[136:139], v161 offset:14336
	ds_read_b128 v[140:143], v161 offset:15360
	s_add_u32 s19, s19, 0x4000
	s_cmp_eq_u32 s19, 0x18000
	s_cselect_b32 s19, 0, s19
	v_add_u32_e32 v161, s19, v160
	s_waitcnt lgkmcnt(4)
	v_mfma_f32_32x32x16_f16 v[16:31], v[144:147], v[112:115], v[16:31]
	v_mfma_f32_32x32x16_f16 v[0:15], v[144:147], v[116:119], v[0:15]
	v_mfma_f32_32x32x16_f16 v[16:31], v[148:151], v[120:123], v[16:31]
	v_mfma_f32_32x32x16_f16 v[0:15], v[148:151], v[124:127], v[0:15]
	s_add_u32 s26, s24, 0x100000
	s_addc_u32 s27, s25, 0
	s_lshl_b32 s45, s43, 16
	s_add_u32 s28, s8, s45
	s_addc_u32 s29, s9, 0
	v_pk_mul_f16 v152, v49, v32 op_sel:[1,0] op_sel_hi:[1,1]
	v_pk_mul_f16 v153, v49, v33 op_sel:[1,0] op_sel_hi:[1,1]
	v_pk_mul_f16 v154, v49, v34 op_sel:[1,0] op_sel_hi:[1,1]
	v_pk_mul_f16 v155, v49, v35 op_sel:[1,0] op_sel_hi:[1,1]
	s_add_u32 s30, s28, 0x100000
	s_addc_u32 s31, s29, 0
	v_pk_fma_f16 v152, v41, v36, v152 op_sel:[1,0,0] op_sel_hi:[1,1,1]
	v_pk_fma_f16 v153, v41, v37, v153 op_sel:[1,0,0] op_sel_hi:[1,1,1]
	v_pk_fma_f16 v154, v41, v38, v154 op_sel:[1,0,0] op_sel_hi:[1,1,1]
	v_pk_fma_f16 v155, v41, v39, v155 op_sel:[1,0,0] op_sel_hi:[1,1,1]
	global_load_dwordx4 v[60:63], v164, s[24:25]
	v_pk_mul_f16 v156, v49, v36 op_sel:[1,0] op_sel_hi:[1,1]
	v_pk_mul_f16 v157, v49, v37 op_sel:[1,0] op_sel_hi:[1,1]
	v_pk_mul_f16 v158, v49, v38 op_sel:[1,0] op_sel_hi:[1,1]
	v_pk_mul_f16 v159, v49, v39 op_sel:[1,0] op_sel_hi:[1,1]
	global_load_dwordx4 v[56:59], v164, s[26:27]
	v_pk_fma_f16 v156, v41, v32, v156 op_sel:[1,0,0] op_sel_hi:[1,1,1] neg_lo:[0,0,1] neg_hi:[0,0,1]
	v_pk_fma_f16 v157, v41, v33, v157 op_sel:[1,0,0] op_sel_hi:[1,1,1] neg_lo:[0,0,1] neg_hi:[0,0,1]
	v_pk_fma_f16 v158, v41, v34, v158 op_sel:[1,0,0] op_sel_hi:[1,1,1] neg_lo:[0,0,1] neg_hi:[0,0,1]
	v_pk_fma_f16 v159, v41, v35, v159 op_sel:[1,0,0] op_sel_hi:[1,1,1] neg_lo:[0,0,1] neg_hi:[0,0,1]
	ds_read_b128 v[80:83], v161
	ds_read_b128 v[84:87], v161 offset:1024
	ds_read_b128 v[88:91], v161 offset:2048
	ds_read_b128 v[92:95], v161 offset:3072
	s_waitcnt lgkmcnt(4)
	v_mfma_f32_32x32x16_f16 v[16:31], v[152:155], v[128:131], v[16:31]
	v_mfma_f32_32x32x16_f16 v[0:15], v[152:155], v[132:135], v[0:15]
	v_mfma_f32_32x32x16_f16 v[16:31], v[156:159], v[136:139], v[16:31]
	v_mfma_f32_32x32x16_f16 v[0:15], v[156:159], v[140:143], v[0:15]
	global_load_dwordx4 v[64:67], v165, s[28:29]
	v_pk_mul_f16 v144, v50, v32 op_sel:[0,0] op_sel_hi:[0,1]
	v_pk_mul_f16 v145, v50, v33 op_sel:[0,0] op_sel_hi:[0,1]
	v_pk_mul_f16 v146, v50, v34 op_sel:[0,0] op_sel_hi:[0,1]
	v_pk_mul_f16 v147, v50, v35 op_sel:[0,0] op_sel_hi:[0,1]
	global_load_dwordx4 v[68:71], v166, s[28:29]
	v_pk_fma_f16 v144, v42, v36, v144 op_sel:[0,0,0] op_sel_hi:[0,1,1]
	v_pk_fma_f16 v145, v42, v37, v145 op_sel:[0,0,0] op_sel_hi:[0,1,1]
	v_pk_fma_f16 v146, v42, v38, v146 op_sel:[0,0,0] op_sel_hi:[0,1,1]
	v_pk_fma_f16 v147, v42, v39, v147 op_sel:[0,0,0] op_sel_hi:[0,1,1]
	global_load_dwordx4 v[72:75], v165, s[30:31]
	v_pk_mul_f16 v148, v50, v36 op_sel:[0,0] op_sel_hi:[0,1]
	v_pk_mul_f16 v149, v50, v37 op_sel:[0,0] op_sel_hi:[0,1]
	v_pk_mul_f16 v150, v50, v38 op_sel:[0,0] op_sel_hi:[0,1]
	v_pk_mul_f16 v151, v50, v39 op_sel:[0,0] op_sel_hi:[0,1]
	global_load_dwordx4 v[76:79], v166, s[30:31]
	v_pk_fma_f16 v148, v42, v32, v148 op_sel:[0,0,0] op_sel_hi:[0,1,1] neg_lo:[0,0,1] neg_hi:[0,0,1]
	v_pk_fma_f16 v149, v42, v33, v149 op_sel:[0,0,0] op_sel_hi:[0,1,1] neg_lo:[0,0,1] neg_hi:[0,0,1]
	v_pk_fma_f16 v150, v42, v34, v150 op_sel:[0,0,0] op_sel_hi:[0,1,1] neg_lo:[0,0,1] neg_hi:[0,0,1]
	v_pk_fma_f16 v151, v42, v35, v151 op_sel:[0,0,0] op_sel_hi:[0,1,1] neg_lo:[0,0,1] neg_hi:[0,0,1]
	ds_read_b128 v[96:99], v161 offset:4096
	ds_read_b128 v[100:103], v161 offset:5120
	ds_read_b128 v[104:107], v161 offset:6144
	ds_read_b128 v[108:111], v161 offset:7168
	s_add_u32 s17, s17, 1
	s_cmp_eq_u32 s17, 17
	s_cbranch_scc1 .Lk2_epi

.Lk2_b01:
	s_waitcnt lgkmcnt(4)
	v_mfma_f32_32x32x16_f16 v[16:31], v[144:147], v[80:83], v[16:31]
	v_mfma_f32_32x32x16_f16 v[0:15], v[144:147], v[84:87], v[0:15]
	v_mfma_f32_32x32x16_f16 v[16:31], v[148:151], v[88:91], v[16:31]
	v_mfma_f32_32x32x16_f16 v[0:15], v[148:151], v[92:95], v[0:15]
	s_cmp_le_u32 s22, 16
	s_cselect_b32 s40, s18, 0x18000
	s_add_u32 m0, s40, s35
	v_pk_mul_f16 v152, v50, v32 op_sel:[1,0] op_sel_hi:[1,1]
	v_pk_mul_f16 v153, v50, v33 op_sel:[1,0] op_sel_hi:[1,1]
	v_pk_mul_f16 v154, v50, v34 op_sel:[1,0] op_sel_hi:[1,1]
	v_pk_mul_f16 v155, v50, v35 op_sel:[1,0] op_sel_hi:[1,1]
	s_add_u32 s22, s22, 1
	global_load_lds_dwordx4 v168, s[20:21]
	global_load_lds_dwordx4 v168, s[20:21] offset:1024
	v_pk_fma_f16 v152, v42, v36, v152 op_sel:[1,0,0] op_sel_hi:[1,1,1]
	v_pk_fma_f16 v153, v42, v37, v153 op_sel:[1,0,0] op_sel_hi:[1,1,1]
	v_pk_fma_f16 v154, v42, v38, v154 op_sel:[1,0,0] op_sel_hi:[1,1,1]
	v_pk_fma_f16 v155, v42, v39, v155 op_sel:[1,0,0] op_sel_hi:[1,1,1]
	s_cmp_le_u32 s22, 16
	s_cselect_b32 s41, 0x4000, 0
	v_pk_mul_f16 v156, v50, v36 op_sel:[1,0] op_sel_hi:[1,1]
	v_pk_mul_f16 v157, v50, v37 op_sel:[1,0] op_sel_hi:[1,1]
	v_pk_mul_f16 v158, v50, v38 op_sel:[1,0] op_sel_hi:[1,1]
	v_pk_mul_f16 v159, v50, v39 op_sel:[1,0] op_sel_hi:[1,1]
	s_add_u32 s20, s20, s41
	s_addc_u32 s21, s21, 0
	v_pk_fma_f16 v156, v42, v32, v156 op_sel:[1,0,0] op_sel_hi:[1,1,1] neg_lo:[0,0,1] neg_hi:[0,0,1]
	v_pk_fma_f16 v157, v42, v33, v157 op_sel:[1,0,0] op_sel_hi:[1,1,1] neg_lo:[0,0,1] neg_hi:[0,0,1]
	v_pk_fma_f16 v158, v42, v34, v158 op_sel:[1,0,0] op_sel_hi:[1,1,1] neg_lo:[0,0,1] neg_hi:[0,0,1]
	v_pk_fma_f16 v159, v42, v35, v159 op_sel:[1,0,0] op_sel_hi:[1,1,1] neg_lo:[0,0,1] neg_hi:[0,0,1]
	ds_read_b128 v[112:115], v161 offset:8192
	ds_read_b128 v[116:119], v161 offset:9216
	ds_read_b128 v[120:123], v161 offset:10240
	ds_read_b128 v[124:127], v161 offset:11264
	s_waitcnt lgkmcnt(4)
	v_mfma_f32_32x32x16_f16 v[16:31], v[152:155], v[96:99], v[16:31]
	v_mfma_f32_32x32x16_f16 v[0:15], v[152:155], v[100:103], v[0:15]
	v_mfma_f32_32x32x16_f16 v[16:31], v[156:159], v[104:107], v[16:31]
	v_mfma_f32_32x32x16_f16 v[0:15], v[156:159], v[108:111], v[0:15]
	s_add_u32 s18, s18, 0x4000
	s_cmp_eq_u32 s18, 0x18000
	s_cselect_b32 s18, 0, s18
	v_pk_mul_f16 v144, v51, v32 op_sel:[0,0] op_sel_hi:[0,1]
	v_pk_mul_f16 v145, v51, v33 op_sel:[0,0] op_sel_hi:[0,1]
	v_pk_mul_f16 v146, v51, v34 op_sel:[0,0] op_sel_hi:[0,1]
	v_pk_mul_f16 v147, v51, v35 op_sel:[0,0] op_sel_hi:[0,1]
	v_pk_fma_f16 v144, v43, v36, v144 op_sel:[0,0,0] op_sel_hi:[0,1,1]
	v_pk_fma_f16 v145, v43, v37, v145 op_sel:[0,0,0] op_sel_hi:[0,1,1]
	v_pk_fma_f16 v146, v43, v38, v146 op_sel:[0,0,0] op_sel_hi:[0,1,1]
	v_pk_fma_f16 v147, v43, v39, v147 op_sel:[0,0,0] op_sel_hi:[0,1,1]
	v_pk_mul_f16 v148, v51, v36 op_sel:[0,0] op_sel_hi:[0,1]
	v_pk_mul_f16 v149, v51, v37 op_sel:[0,0] op_sel_hi:[0,1]
	v_pk_mul_f16 v150, v51, v38 op_sel:[0,0] op_sel_hi:[0,1]
	v_pk_mul_f16 v151, v51, v39 op_sel:[0,0] op_sel_hi:[0,1]
	v_pk_fma_f16 v148, v43, v32, v148 op_sel:[0,0,0] op_sel_hi:[0,1,1] neg_lo:[0,0,1] neg_hi:[0,0,1]
	v_pk_fma_f16 v149, v43, v33, v149 op_sel:[0,0,0] op_sel_hi:[0,1,1] neg_lo:[0,0,1] neg_hi:[0,0,1]
	v_pk_fma_f16 v150, v43, v34, v150 op_sel:[0,0,0] op_sel_hi:[0,1,1] neg_lo:[0,0,1] neg_hi:[0,0,1]
	v_pk_fma_f16 v151, v43, v35, v151 op_sel:[0,0,0] op_sel_hi:[0,1,1] neg_lo:[0,0,1] neg_hi:[0,0,1]
	ds_read_b128 v[128:131], v161 offset:12288
	ds_read_b128 v[132:135], v161 offset:13312
	ds_read_b128 v[136:139], v161 offset:14336
	ds_read_b128 v[140:143], v161 offset:15360
	s_add_u32 s19, s19, 0x4000
	s_cmp_eq_u32 s19, 0x18000
	s_cselect_b32 s19, 0, s19
	v_add_u32_e32 v161, s19, v160
	s_waitcnt lgkmcnt(4)
	v_mfma_f32_32x32x16_f16 v[16:31], v[144:147], v[112:115], v[16:31]
	v_mfma_f32_32x32x16_f16 v[0:15], v[144:147], v[116:119], v[0:15]
	v_mfma_f32_32x32x16_f16 v[16:31], v[148:151], v[120:123], v[16:31]
	v_mfma_f32_32x32x16_f16 v[0:15], v[148:151], v[124:127], v[0:15]
	v_pk_mul_f16 v152, v51, v32 op_sel:[1,0] op_sel_hi:[1,1]
	v_pk_mul_f16 v153, v51, v33 op_sel:[1,0] op_sel_hi:[1,1]
	v_pk_mul_f16 v154, v51, v34 op_sel:[1,0] op_sel_hi:[1,1]
	v_pk_mul_f16 v155, v51, v35 op_sel:[1,0] op_sel_hi:[1,1]
	v_pk_fma_f16 v152, v43, v36, v152 op_sel:[1,0,0] op_sel_hi:[1,1,1]
	v_pk_fma_f16 v153, v43, v37, v153 op_sel:[1,0,0] op_sel_hi:[1,1,1]
	v_pk_fma_f16 v154, v43, v38, v154 op_sel:[1,0,0] op_sel_hi:[1,1,1]
	v_pk_fma_f16 v155, v43, v39, v155 op_sel:[1,0,0] op_sel_hi:[1,1,1]
	v_pk_mul_f16 v156, v51, v36 op_sel:[1,0] op_sel_hi:[1,1]
	v_pk_mul_f16 v157, v51, v37 op_sel:[1,0] op_sel_hi:[1,1]
	v_pk_mul_f16 v158, v51, v38 op_sel:[1,0] op_sel_hi:[1,1]
	v_pk_mul_f16 v159, v51, v39 op_sel:[1,0] op_sel_hi:[1,1]
	v_pk_fma_f16 v156, v43, v32, v156 op_sel:[1,0,0] op_sel_hi:[1,1,1] neg_lo:[0,0,1] neg_hi:[0,0,1]
	v_pk_fma_f16 v157, v43, v33, v157 op_sel:[1,0,0] op_sel_hi:[1,1,1] neg_lo:[0,0,1] neg_hi:[0,0,1]
	v_pk_fma_f16 v158, v43, v34, v158 op_sel:[1,0,0] op_sel_hi:[1,1,1] neg_lo:[0,0,1] neg_hi:[0,0,1]
	v_pk_fma_f16 v159, v43, v35, v159 op_sel:[1,0,0] op_sel_hi:[1,1,1] neg_lo:[0,0,1] neg_hi:[0,0,1]
	ds_read_b128 v[80:83], v161
	ds_read_b128 v[84:87], v161 offset:1024
	ds_read_b128 v[88:91], v161 offset:2048
	ds_read_b128 v[92:95], v161 offset:3072
	s_waitcnt lgkmcnt(4)
	v_mfma_f32_32x32x16_f16 v[16:31], v[152:155], v[128:131], v[16:31]
	v_mfma_f32_32x32x16_f16 v[0:15], v[152:155], v[132:135], v[0:15]
	v_mfma_f32_32x32x16_f16 v[16:31], v[156:159], v[136:139], v[16:31]
	v_mfma_f32_32x32x16_f16 v[0:15], v[156:159], v[140:143], v[0:15]
	v_pk_mul_f16 v144, v52, v32 op_sel:[0,0] op_sel_hi:[0,1]
	v_pk_mul_f16 v145, v52, v33 op_sel:[0,0] op_sel_hi:[0,1]
	v_pk_mul_f16 v146, v52, v34 op_sel:[0,0] op_sel_hi:[0,1]
	v_pk_mul_f16 v147, v52, v35 op_sel:[0,0] op_sel_hi:[0,1]
	v_pk_fma_f16 v144, v44, v36, v144 op_sel:[0,0,0] op_sel_hi:[0,1,1]
	v_pk_fma_f16 v145, v44, v37, v145 op_sel:[0,0,0] op_sel_hi:[0,1,1]
	v_pk_fma_f16 v146, v44, v38, v146 op_sel:[0,0,0] op_sel_hi:[0,1,1]
	v_pk_fma_f16 v147, v44, v39, v147 op_sel:[0,0,0] op_sel_hi:[0,1,1]
	v_pk_mul_f16 v148, v52, v36 op_sel:[0,0] op_sel_hi:[0,1]
	v_pk_mul_f16 v149, v52, v37 op_sel:[0,0] op_sel_hi:[0,1]
	v_pk_mul_f16 v150, v52, v38 op_sel:[0,0] op_sel_hi:[0,1]
	v_pk_mul_f16 v151, v52, v39 op_sel:[0,0] op_sel_hi:[0,1]
	v_pk_fma_f16 v148, v44, v32, v148 op_sel:[0,0,0] op_sel_hi:[0,1,1] neg_lo:[0,0,1] neg_hi:[0,0,1]
	v_pk_fma_f16 v149, v44, v33, v149 op_sel:[0,0,0] op_sel_hi:[0,1,1] neg_lo:[0,0,1] neg_hi:[0,0,1]
	v_pk_fma_f16 v150, v44, v34, v150 op_sel:[0,0,0] op_sel_hi:[0,1,1] neg_lo:[0,0,1] neg_hi:[0,0,1]
	v_pk_fma_f16 v151, v44, v35, v151 op_sel:[0,0,0] op_sel_hi:[0,1,1] neg_lo:[0,0,1] neg_hi:[0,0,1]
	ds_read_b128 v[96:99], v161 offset:4096
	ds_read_b128 v[100:103], v161 offset:5120
	ds_read_b128 v[104:107], v161 offset:6144
	ds_read_b128 v[108:111], v161 offset:7168
	s_add_u32 s17, s17, 1
	s_cmp_eq_u32 s17, 17
	s_cbranch_scc1 .Lk2_epi

.Lk2_b02:
	s_waitcnt lgkmcnt(4)
	v_mfma_f32_32x32x16_f16 v[16:31], v[144:147], v[80:83], v[16:31]
	v_mfma_f32_32x32x16_f16 v[0:15], v[144:147], v[84:87], v[0:15]
	v_mfma_f32_32x32x16_f16 v[16:31], v[148:151], v[88:91], v[16:31]
	v_mfma_f32_32x32x16_f16 v[0:15], v[148:151], v[92:95], v[0:15]
	s_cmp_le_u32 s22, 16
	s_cselect_b32 s40, s18, 0x18000
	s_add_u32 m0, s40, s35
	v_pk_mul_f16 v152, v52, v32 op_sel:[1,0] op_sel_hi:[1,1]
	v_pk_mul_f16 v153, v52, v33 op_sel:[1,0] op_sel_hi:[1,1]
	v_pk_mul_f16 v154, v52, v34 op_sel:[1,0] op_sel_hi:[1,1]
	v_pk_mul_f16 v155, v52, v35 op_sel:[1,0] op_sel_hi:[1,1]
	s_add_u32 s22, s22, 1
	global_load_lds_dwordx4 v168, s[20:21]
	global_load_lds_dwordx4 v168, s[20:21] offset:1024
	v_pk_fma_f16 v152, v44, v36, v152 op_sel:[1,0,0] op_sel_hi:[1,1,1]
	v_pk_fma_f16 v153, v44, v37, v153 op_sel:[1,0,0] op_sel_hi:[1,1,1]
	v_pk_fma_f16 v154, v44, v38, v154 op_sel:[1,0,0] op_sel_hi:[1,1,1]
	v_pk_fma_f16 v155, v44, v39, v155 op_sel:[1,0,0] op_sel_hi:[1,1,1]
	s_cmp_le_u32 s22, 16
	s_cselect_b32 s41, 0x4000, 0
	v_pk_mul_f16 v156, v52, v36 op_sel:[1,0] op_sel_hi:[1,1]
	v_pk_mul_f16 v157, v52, v37 op_sel:[1,0] op_sel_hi:[1,1]
	v_pk_mul_f16 v158, v52, v38 op_sel:[1,0] op_sel_hi:[1,1]
	v_pk_mul_f16 v159, v52, v39 op_sel:[1,0] op_sel_hi:[1,1]
	s_add_u32 s20, s20, s41
	s_addc_u32 s21, s21, 0
	v_pk_fma_f16 v156, v44, v32, v156 op_sel:[1,0,0] op_sel_hi:[1,1,1] neg_lo:[0,0,1] neg_hi:[0,0,1]
	v_pk_fma_f16 v157, v44, v33, v157 op_sel:[1,0,0] op_sel_hi:[1,1,1] neg_lo:[0,0,1] neg_hi:[0,0,1]
	v_pk_fma_f16 v158, v44, v34, v158 op_sel:[1,0,0] op_sel_hi:[1,1,1] neg_lo:[0,0,1] neg_hi:[0,0,1]
	v_pk_fma_f16 v159, v44, v35, v159 op_sel:[1,0,0] op_sel_hi:[1,1,1] neg_lo:[0,0,1] neg_hi:[0,0,1]
	ds_read_b128 v[112:115], v161 offset:8192
	ds_read_b128 v[116:119], v161 offset:9216
	ds_read_b128 v[120:123], v161 offset:10240
	ds_read_b128 v[124:127], v161 offset:11264
	s_waitcnt lgkmcnt(4)
	v_mfma_f32_32x32x16_f16 v[16:31], v[152:155], v[96:99], v[16:31]
	v_mfma_f32_32x32x16_f16 v[0:15], v[152:155], v[100:103], v[0:15]
	v_mfma_f32_32x32x16_f16 v[16:31], v[156:159], v[104:107], v[16:31]
	v_mfma_f32_32x32x16_f16 v[0:15], v[156:159], v[108:111], v[0:15]
	s_add_u32 s18, s18, 0x4000
	s_cmp_eq_u32 s18, 0x18000
	s_cselect_b32 s18, 0, s18
	v_pk_mul_f16 v144, v53, v32 op_sel:[0,0] op_sel_hi:[0,1]
	v_pk_mul_f16 v145, v53, v33 op_sel:[0,0] op_sel_hi:[0,1]
	v_pk_mul_f16 v146, v53, v34 op_sel:[0,0] op_sel_hi:[0,1]
	v_pk_mul_f16 v147, v53, v35 op_sel:[0,0] op_sel_hi:[0,1]
	v_pk_fma_f16 v144, v45, v36, v144 op_sel:[0,0,0] op_sel_hi:[0,1,1]
	v_pk_fma_f16 v145, v45, v37, v145 op_sel:[0,0,0] op_sel_hi:[0,1,1]
	v_pk_fma_f16 v146, v45, v38, v146 op_sel:[0,0,0] op_sel_hi:[0,1,1]
	v_pk_fma_f16 v147, v45, v39, v147 op_sel:[0,0,0] op_sel_hi:[0,1,1]
	v_pk_mul_f16 v148, v53, v36 op_sel:[0,0] op_sel_hi:[0,1]
	v_pk_mul_f16 v149, v53, v37 op_sel:[0,0] op_sel_hi:[0,1]
	v_pk_mul_f16 v150, v53, v38 op_sel:[0,0] op_sel_hi:[0,1]
	v_pk_mul_f16 v151, v53, v39 op_sel:[0,0] op_sel_hi:[0,1]
	v_pk_fma_f16 v148, v45, v32, v148 op_sel:[0,0,0] op_sel_hi:[0,1,1] neg_lo:[0,0,1] neg_hi:[0,0,1]
	v_pk_fma_f16 v149, v45, v33, v149 op_sel:[0,0,0] op_sel_hi:[0,1,1] neg_lo:[0,0,1] neg_hi:[0,0,1]
	v_pk_fma_f16 v150, v45, v34, v150 op_sel:[0,0,0] op_sel_hi:[0,1,1] neg_lo:[0,0,1] neg_hi:[0,0,1]
	v_pk_fma_f16 v151, v45, v35, v151 op_sel:[0,0,0] op_sel_hi:[0,1,1] neg_lo:[0,0,1] neg_hi:[0,0,1]
	ds_read_b128 v[128:131], v161 offset:12288
	ds_read_b128 v[132:135], v161 offset:13312
	ds_read_b128 v[136:139], v161 offset:14336
	ds_read_b128 v[140:143], v161 offset:15360
	s_add_u32 s19, s19, 0x4000
	s_cmp_eq_u32 s19, 0x18000
	s_cselect_b32 s19, 0, s19
	v_add_u32_e32 v161, s19, v160
	s_waitcnt lgkmcnt(4)
	v_mfma_f32_32x32x16_f16 v[16:31], v[144:147], v[112:115], v[16:31]
	v_mfma_f32_32x32x16_f16 v[0:15], v[144:147], v[116:119], v[0:15]
	v_mfma_f32_32x32x16_f16 v[16:31], v[148:151], v[120:123], v[16:31]
	v_mfma_f32_32x32x16_f16 v[0:15], v[148:151], v[124:127], v[0:15]
	v_pk_mul_f16 v152, v53, v32 op_sel:[1,0] op_sel_hi:[1,1]
	v_pk_mul_f16 v153, v53, v33 op_sel:[1,0] op_sel_hi:[1,1]
	v_pk_mul_f16 v154, v53, v34 op_sel:[1,0] op_sel_hi:[1,1]
	v_pk_mul_f16 v155, v53, v35 op_sel:[1,0] op_sel_hi:[1,1]
	v_pk_fma_f16 v152, v45, v36, v152 op_sel:[1,0,0] op_sel_hi:[1,1,1]
	v_pk_fma_f16 v153, v45, v37, v153 op_sel:[1,0,0] op_sel_hi:[1,1,1]
	v_pk_fma_f16 v154, v45, v38, v154 op_sel:[1,0,0] op_sel_hi:[1,1,1]
	v_pk_fma_f16 v155, v45, v39, v155 op_sel:[1,0,0] op_sel_hi:[1,1,1]
	v_pk_mul_f16 v156, v53, v36 op_sel:[1,0] op_sel_hi:[1,1]
	v_pk_mul_f16 v157, v53, v37 op_sel:[1,0] op_sel_hi:[1,1]
	v_pk_mul_f16 v158, v53, v38 op_sel:[1,0] op_sel_hi:[1,1]
	v_pk_mul_f16 v159, v53, v39 op_sel:[1,0] op_sel_hi:[1,1]
	v_pk_fma_f16 v156, v45, v32, v156 op_sel:[1,0,0] op_sel_hi:[1,1,1] neg_lo:[0,0,1] neg_hi:[0,0,1]
	v_pk_fma_f16 v157, v45, v33, v157 op_sel:[1,0,0] op_sel_hi:[1,1,1] neg_lo:[0,0,1] neg_hi:[0,0,1]
	v_pk_fma_f16 v158, v45, v34, v158 op_sel:[1,0,0] op_sel_hi:[1,1,1] neg_lo:[0,0,1] neg_hi:[0,0,1]
	v_pk_fma_f16 v159, v45, v35, v159 op_sel:[1,0,0] op_sel_hi:[1,1,1] neg_lo:[0,0,1] neg_hi:[0,0,1]
	ds_read_b128 v[80:83], v161
	ds_read_b128 v[84:87], v161 offset:1024
	ds_read_b128 v[88:91], v161 offset:2048
	ds_read_b128 v[92:95], v161 offset:3072
	s_waitcnt lgkmcnt(4)
	v_mfma_f32_32x32x16_f16 v[16:31], v[152:155], v[128:131], v[16:31]
	v_mfma_f32_32x32x16_f16 v[0:15], v[152:155], v[132:135], v[0:15]
	v_mfma_f32_32x32x16_f16 v[16:31], v[156:159], v[136:139], v[16:31]
	v_mfma_f32_32x32x16_f16 v[0:15], v[156:159], v[140:143], v[0:15]
	v_pk_mul_f16 v144, v54, v32 op_sel:[0,0] op_sel_hi:[0,1]
	v_pk_mul_f16 v145, v54, v33 op_sel:[0,0] op_sel_hi:[0,1]
	v_pk_mul_f16 v146, v54, v34 op_sel:[0,0] op_sel_hi:[0,1]
	v_pk_mul_f16 v147, v54, v35 op_sel:[0,0] op_sel_hi:[0,1]
	v_pk_fma_f16 v144, v46, v36, v144 op_sel:[0,0,0] op_sel_hi:[0,1,1]
	v_pk_fma_f16 v145, v46, v37, v145 op_sel:[0,0,0] op_sel_hi:[0,1,1]
	v_pk_fma_f16 v146, v46, v38, v146 op_sel:[0,0,0] op_sel_hi:[0,1,1]
	v_pk_fma_f16 v147, v46, v39, v147 op_sel:[0,0,0] op_sel_hi:[0,1,1]
	v_pk_mul_f16 v148, v54, v36 op_sel:[0,0] op_sel_hi:[0,1]
	v_pk_mul_f16 v149, v54, v37 op_sel:[0,0] op_sel_hi:[0,1]
	v_pk_mul_f16 v150, v54, v38 op_sel:[0,0] op_sel_hi:[0,1]
	v_pk_mul_f16 v151, v54, v39 op_sel:[0,0] op_sel_hi:[0,1]
	v_pk_fma_f16 v148, v46, v32, v148 op_sel:[0,0,0] op_sel_hi:[0,1,1] neg_lo:[0,0,1] neg_hi:[0,0,1]
	v_pk_fma_f16 v149, v46, v33, v149 op_sel:[0,0,0] op_sel_hi:[0,1,1] neg_lo:[0,0,1] neg_hi:[0,0,1]
	v_pk_fma_f16 v150, v46, v34, v150 op_sel:[0,0,0] op_sel_hi:[0,1,1] neg_lo:[0,0,1] neg_hi:[0,0,1]
	v_pk_fma_f16 v151, v46, v35, v151 op_sel:[0,0,0] op_sel_hi:[0,1,1] neg_lo:[0,0,1] neg_hi:[0,0,1]
	ds_read_b128 v[96:99], v161 offset:4096
	ds_read_b128 v[100:103], v161 offset:5120
	ds_read_b128 v[104:107], v161 offset:6144
	ds_read_b128 v[108:111], v161 offset:7168
	s_add_u32 s17, s17, 1
	s_cmp_eq_u32 s17, 17
	s_cbranch_scc1 .Lk2_epi

.Lk2_b03:
	s_waitcnt lgkmcnt(4)
	v_mfma_f32_32x32x16_f16 v[16:31], v[144:147], v[80:83], v[16:31]
	v_mfma_f32_32x32x16_f16 v[0:15], v[144:147], v[84:87], v[0:15]
	v_mfma_f32_32x32x16_f16 v[16:31], v[148:151], v[88:91], v[16:31]
	v_mfma_f32_32x32x16_f16 v[0:15], v[148:151], v[92:95], v[0:15]
	s_cmp_le_u32 s22, 16
	s_cselect_b32 s40, s18, 0x18000
	s_add_u32 m0, s40, s35
	v_pk_mul_f16 v152, v54, v32 op_sel:[1,0] op_sel_hi:[1,1]
	v_pk_mul_f16 v153, v54, v33 op_sel:[1,0] op_sel_hi:[1,1]
	v_pk_mul_f16 v154, v54, v34 op_sel:[1,0] op_sel_hi:[1,1]
	v_pk_mul_f16 v155, v54, v35 op_sel:[1,0] op_sel_hi:[1,1]
	s_add_u32 s22, s22, 1
	global_load_lds_dwordx4 v168, s[20:21]
	global_load_lds_dwordx4 v168, s[20:21] offset:1024
	v_pk_fma_f16 v152, v46, v36, v152 op_sel:[1,0,0] op_sel_hi:[1,1,1]
	v_pk_fma_f16 v153, v46, v37, v153 op_sel:[1,0,0] op_sel_hi:[1,1,1]
	v_pk_fma_f16 v154, v46, v38, v154 op_sel:[1,0,0] op_sel_hi:[1,1,1]
	v_pk_fma_f16 v155, v46, v39, v155 op_sel:[1,0,0] op_sel_hi:[1,1,1]
	s_cmp_le_u32 s22, 16
	s_cselect_b32 s41, 0x4000, 0
	v_pk_mul_f16 v156, v54, v36 op_sel:[1,0] op_sel_hi:[1,1]
	v_pk_mul_f16 v157, v54, v37 op_sel:[1,0] op_sel_hi:[1,1]
	v_pk_mul_f16 v158, v54, v38 op_sel:[1,0] op_sel_hi:[1,1]
	v_pk_mul_f16 v159, v54, v39 op_sel:[1,0] op_sel_hi:[1,1]
	s_add_u32 s20, s20, s41
	s_addc_u32 s21, s21, 0
	v_pk_fma_f16 v156, v46, v32, v156 op_sel:[1,0,0] op_sel_hi:[1,1,1] neg_lo:[0,0,1] neg_hi:[0,0,1]
	v_pk_fma_f16 v157, v46, v33, v157 op_sel:[1,0,0] op_sel_hi:[1,1,1] neg_lo:[0,0,1] neg_hi:[0,0,1]
	v_pk_fma_f16 v158, v46, v34, v158 op_sel:[1,0,0] op_sel_hi:[1,1,1] neg_lo:[0,0,1] neg_hi:[0,0,1]
	v_pk_fma_f16 v159, v46, v35, v159 op_sel:[1,0,0] op_sel_hi:[1,1,1] neg_lo:[0,0,1] neg_hi:[0,0,1]
	ds_read_b128 v[112:115], v161 offset:8192
	ds_read_b128 v[116:119], v161 offset:9216
	ds_read_b128 v[120:123], v161 offset:10240
	ds_read_b128 v[124:127], v161 offset:11264
	s_waitcnt lgkmcnt(4)
	v_mfma_f32_32x32x16_f16 v[16:31], v[152:155], v[96:99], v[16:31]
	v_mfma_f32_32x32x16_f16 v[0:15], v[152:155], v[100:103], v[0:15]
	v_mfma_f32_32x32x16_f16 v[16:31], v[156:159], v[104:107], v[16:31]
	v_mfma_f32_32x32x16_f16 v[0:15], v[156:159], v[108:111], v[0:15]
	s_add_u32 s18, s18, 0x4000
	s_cmp_eq_u32 s18, 0x18000
	s_cselect_b32 s18, 0, s18
	v_pk_mul_f16 v144, v55, v32 op_sel:[0,0] op_sel_hi:[0,1]
	v_pk_mul_f16 v145, v55, v33 op_sel:[0,0] op_sel_hi:[0,1]
	v_pk_mul_f16 v146, v55, v34 op_sel:[0,0] op_sel_hi:[0,1]
	v_pk_mul_f16 v147, v55, v35 op_sel:[0,0] op_sel_hi:[0,1]
	v_pk_fma_f16 v144, v47, v36, v144 op_sel:[0,0,0] op_sel_hi:[0,1,1]
	v_pk_fma_f16 v145, v47, v37, v145 op_sel:[0,0,0] op_sel_hi:[0,1,1]
	v_pk_fma_f16 v146, v47, v38, v146 op_sel:[0,0,0] op_sel_hi:[0,1,1]
	v_pk_fma_f16 v147, v47, v39, v147 op_sel:[0,0,0] op_sel_hi:[0,1,1]
	v_pk_mul_f16 v148, v55, v36 op_sel:[0,0] op_sel_hi:[0,1]
	v_pk_mul_f16 v149, v55, v37 op_sel:[0,0] op_sel_hi:[0,1]
	v_pk_mul_f16 v150, v55, v38 op_sel:[0,0] op_sel_hi:[0,1]
	v_pk_mul_f16 v151, v55, v39 op_sel:[0,0] op_sel_hi:[0,1]
	v_pk_fma_f16 v148, v47, v32, v148 op_sel:[0,0,0] op_sel_hi:[0,1,1] neg_lo:[0,0,1] neg_hi:[0,0,1]
	v_pk_fma_f16 v149, v47, v33, v149 op_sel:[0,0,0] op_sel_hi:[0,1,1] neg_lo:[0,0,1] neg_hi:[0,0,1]
	v_pk_fma_f16 v150, v47, v34, v150 op_sel:[0,0,0] op_sel_hi:[0,1,1] neg_lo:[0,0,1] neg_hi:[0,0,1]
	v_pk_fma_f16 v151, v47, v35, v151 op_sel:[0,0,0] op_sel_hi:[0,1,1] neg_lo:[0,0,1] neg_hi:[0,0,1]
	ds_read_b128 v[128:131], v161 offset:12288
	ds_read_b128 v[132:135], v161 offset:13312
	ds_read_b128 v[136:139], v161 offset:14336
	ds_read_b128 v[140:143], v161 offset:15360
	s_add_u32 s19, s19, 0x4000
	s_cmp_eq_u32 s19, 0x18000
	s_cselect_b32 s19, 0, s19
	v_add_u32_e32 v161, s19, v160
	s_waitcnt lgkmcnt(4)
	v_mfma_f32_32x32x16_f16 v[16:31], v[144:147], v[112:115], v[16:31]
	v_mfma_f32_32x32x16_f16 v[0:15], v[144:147], v[116:119], v[0:15]
	v_mfma_f32_32x32x16_f16 v[16:31], v[148:151], v[120:123], v[16:31]
	v_mfma_f32_32x32x16_f16 v[0:15], v[148:151], v[124:127], v[0:15]
	v_pk_mul_f16 v152, v55, v32 op_sel:[1,0] op_sel_hi:[1,1]
	v_pk_mul_f16 v153, v55, v33 op_sel:[1,0] op_sel_hi:[1,1]
	v_pk_mul_f16 v154, v55, v34 op_sel:[1,0] op_sel_hi:[1,1]
	v_pk_mul_f16 v155, v55, v35 op_sel:[1,0] op_sel_hi:[1,1]
	v_pk_fma_f16 v152, v47, v36, v152 op_sel:[1,0,0] op_sel_hi:[1,1,1]
	v_pk_fma_f16 v153, v47, v37, v153 op_sel:[1,0,0] op_sel_hi:[1,1,1]
	v_pk_fma_f16 v154, v47, v38, v154 op_sel:[1,0,0] op_sel_hi:[1,1,1]
	v_pk_fma_f16 v155, v47, v39, v155 op_sel:[1,0,0] op_sel_hi:[1,1,1]
	v_pk_mul_f16 v156, v55, v36 op_sel:[1,0] op_sel_hi:[1,1]
	v_pk_mul_f16 v157, v55, v37 op_sel:[1,0] op_sel_hi:[1,1]
	v_pk_mul_f16 v158, v55, v38 op_sel:[1,0] op_sel_hi:[1,1]
	v_pk_mul_f16 v159, v55, v39 op_sel:[1,0] op_sel_hi:[1,1]
	v_pk_fma_f16 v156, v47, v32, v156 op_sel:[1,0,0] op_sel_hi:[1,1,1] neg_lo:[0,0,1] neg_hi:[0,0,1]
	v_pk_fma_f16 v157, v47, v33, v157 op_sel:[1,0,0] op_sel_hi:[1,1,1] neg_lo:[0,0,1] neg_hi:[0,0,1]
	v_pk_fma_f16 v158, v47, v34, v158 op_sel:[1,0,0] op_sel_hi:[1,1,1] neg_lo:[0,0,1] neg_hi:[0,0,1]
	v_pk_fma_f16 v159, v47, v35, v159 op_sel:[1,0,0] op_sel_hi:[1,1,1] neg_lo:[0,0,1] neg_hi:[0,0,1]
	ds_read_b128 v[80:83], v161
	ds_read_b128 v[84:87], v161 offset:1024
	ds_read_b128 v[88:91], v161 offset:2048
	ds_read_b128 v[92:95], v161 offset:3072
	s_waitcnt lgkmcnt(4)
	v_mfma_f32_32x32x16_f16 v[16:31], v[152:155], v[128:131], v[16:31]
	v_mfma_f32_32x32x16_f16 v[0:15], v[152:155], v[132:135], v[0:15]
	v_mfma_f32_32x32x16_f16 v[16:31], v[156:159], v[136:139], v[16:31]
	v_mfma_f32_32x32x16_f16 v[0:15], v[156:159], v[140:143], v[0:15]
	s_waitcnt vmcnt(6)
	v_pk_mul_f16 v144, v72, v56 op_sel:[0,0] op_sel_hi:[0,1]
	v_pk_mul_f16 v145, v72, v57 op_sel:[0,0] op_sel_hi:[0,1]
	v_pk_mul_f16 v146, v72, v58 op_sel:[0,0] op_sel_hi:[0,1]
	v_pk_mul_f16 v147, v72, v59 op_sel:[0,0] op_sel_hi:[0,1]
	v_pk_fma_f16 v144, v64, v60, v144 op_sel:[0,0,0] op_sel_hi:[0,1,1]
	v_pk_fma_f16 v145, v64, v61, v145 op_sel:[0,0,0] op_sel_hi:[0,1,1]
	v_pk_fma_f16 v146, v64, v62, v146 op_sel:[0,0,0] op_sel_hi:[0,1,1]
	v_pk_fma_f16 v147, v64, v63, v147 op_sel:[0,0,0] op_sel_hi:[0,1,1]
	v_pk_mul_f16 v148, v72, v60 op_sel:[0,0] op_sel_hi:[0,1]
	v_pk_mul_f16 v149, v72, v61 op_sel:[0,0] op_sel_hi:[0,1]
	v_pk_mul_f16 v150, v72, v62 op_sel:[0,0] op_sel_hi:[0,1]
	v_pk_mul_f16 v151, v72, v63 op_sel:[0,0] op_sel_hi:[0,1]
	v_pk_fma_f16 v148, v64, v56, v148 op_sel:[0,0,0] op_sel_hi:[0,1,1] neg_lo:[0,0,1] neg_hi:[0,0,1]
	v_pk_fma_f16 v149, v64, v57, v149 op_sel:[0,0,0] op_sel_hi:[0,1,1] neg_lo:[0,0,1] neg_hi:[0,0,1]
	v_pk_fma_f16 v150, v64, v58, v150 op_sel:[0,0,0] op_sel_hi:[0,1,1] neg_lo:[0,0,1] neg_hi:[0,0,1]
	v_pk_fma_f16 v151, v64, v59, v151 op_sel:[0,0,0] op_sel_hi:[0,1,1] neg_lo:[0,0,1] neg_hi:[0,0,1]
	ds_read_b128 v[96:99], v161 offset:4096
	ds_read_b128 v[100:103], v161 offset:5120
	ds_read_b128 v[104:107], v161 offset:6144
	ds_read_b128 v[108:111], v161 offset:7168
	s_add_u32 s17, s17, 1
	s_cmp_eq_u32 s17, 17
	s_cbranch_scc1 .Lk2_epi

.Lk2_b10:
	s_waitcnt lgkmcnt(4)
	v_mfma_f32_32x32x16_f16 v[16:31], v[144:147], v[80:83], v[16:31]
	v_mfma_f32_32x32x16_f16 v[0:15], v[144:147], v[84:87], v[0:15]
	v_mfma_f32_32x32x16_f16 v[16:31], v[148:151], v[88:91], v[16:31]
	v_mfma_f32_32x32x16_f16 v[0:15], v[148:151], v[92:95], v[0:15]
	s_cmp_le_u32 s22, 16
	s_cselect_b32 s40, s18, 0x18000
	s_add_u32 m0, s40, s35
	s_add_u32 s22, s22, 1
	global_load_lds_dwordx4 v168, s[20:21]
	global_load_lds_dwordx4 v168, s[20:21] offset:1024
	v_pk_mul_f16 v152, v72, v56 op_sel:[1,0] op_sel_hi:[1,1]
	v_pk_mul_f16 v153, v72, v57 op_sel:[1,0] op_sel_hi:[1,1]
	v_pk_mul_f16 v154, v72, v58 op_sel:[1,0] op_sel_hi:[1,1]
	v_pk_mul_f16 v155, v72, v59 op_sel:[1,0] op_sel_hi:[1,1]
	s_cmp_le_u32 s22, 16
	s_cselect_b32 s41, 0x4000, 0
	v_pk_fma_f16 v152, v64, v60, v152 op_sel:[1,0,0] op_sel_hi:[1,1,1]
	v_pk_fma_f16 v153, v64, v61, v153 op_sel:[1,0,0] op_sel_hi:[1,1,1]
	v_pk_fma_f16 v154, v64, v62, v154 op_sel:[1,0,0] op_sel_hi:[1,1,1]
	v_pk_fma_f16 v155, v64, v63, v155 op_sel:[1,0,0] op_sel_hi:[1,1,1]
	s_add_u32 s20, s20, s41
	s_addc_u32 s21, s21, 0
	v_pk_mul_f16 v156, v72, v60 op_sel:[1,0] op_sel_hi:[1,1]
	v_pk_mul_f16 v157, v72, v61 op_sel:[1,0] op_sel_hi:[1,1]
	v_pk_mul_f16 v158, v72, v62 op_sel:[1,0] op_sel_hi:[1,1]
	v_pk_mul_f16 v159, v72, v63 op_sel:[1,0] op_sel_hi:[1,1]
	s_add_u32 s18, s18, 0x4000
	s_cmp_eq_u32 s18, 0x18000
	s_cselect_b32 s18, 0, s18
	v_pk_fma_f16 v156, v64, v56, v156 op_sel:[1,0,0] op_sel_hi:[1,1,1] neg_lo:[0,0,1] neg_hi:[0,0,1]
	v_pk_fma_f16 v157, v64, v57, v157 op_sel:[1,0,0] op_sel_hi:[1,1,1] neg_lo:[0,0,1] neg_hi:[0,0,1]
	v_pk_fma_f16 v158, v64, v58, v158 op_sel:[1,0,0] op_sel_hi:[1,1,1] neg_lo:[0,0,1] neg_hi:[0,0,1]
	v_pk_fma_f16 v159, v64, v59, v159 op_sel:[1,0,0] op_sel_hi:[1,1,1] neg_lo:[0,0,1] neg_hi:[0,0,1]
	ds_read_b128 v[112:115], v161 offset:8192
	ds_read_b128 v[116:119], v161 offset:9216
	ds_read_b128 v[120:123], v161 offset:10240
	ds_read_b128 v[124:127], v161 offset:11264
	s_waitcnt lgkmcnt(4)
	v_mfma_f32_32x32x16_f16 v[16:31], v[152:155], v[96:99], v[16:31]
	v_mfma_f32_32x32x16_f16 v[0:15], v[152:155], v[100:103], v[0:15]
	v_mfma_f32_32x32x16_f16 v[16:31], v[156:159], v[104:107], v[16:31]
	v_mfma_f32_32x32x16_f16 v[0:15], v[156:159], v[108:111], v[0:15]
	s_add_u32 s14, s14, 1
	s_cmp_eq_u32 s14, 16
	s_cselect_b32 s42, 1, 0
	v_pk_mul_f16 v144, v73, v56 op_sel:[0,0] op_sel_hi:[0,1]
	v_pk_mul_f16 v145, v73, v57 op_sel:[0,0] op_sel_hi:[0,1]
	v_pk_mul_f16 v146, v73, v58 op_sel:[0,0] op_sel_hi:[0,1]
	v_pk_mul_f16 v147, v73, v59 op_sel:[0,0] op_sel_hi:[0,1]
	s_add_u32 s13, s13, s42
	s_cmp_eq_u32 s42, 1
	s_cselect_b32 s14, s13, s14
	v_pk_fma_f16 v144, v65, v60, v144 op_sel:[0,0,0] op_sel_hi:[0,1,1]
	v_pk_fma_f16 v145, v65, v61, v145 op_sel:[0,0,0] op_sel_hi:[0,1,1]
	v_pk_fma_f16 v146, v65, v62, v146 op_sel:[0,0,0] op_sel_hi:[0,1,1]
	v_pk_fma_f16 v147, v65, v63, v147 op_sel:[0,0,0] op_sel_hi:[0,1,1]
	s_min_u32 s43, s13, 15
	s_min_u32 s44, s14, 15
	s_lshl_b32 s45, s44, 16
	v_pk_mul_f16 v148, v73, v60 op_sel:[0,0] op_sel_hi:[0,1]
	v_pk_mul_f16 v149, v73, v61 op_sel:[0,0] op_sel_hi:[0,1]
	v_pk_mul_f16 v150, v73, v62 op_sel:[0,0] op_sel_hi:[0,1]
	v_pk_mul_f16 v151, v73, v63 op_sel:[0,0] op_sel_hi:[0,1]
	s_add_u32 s24, s8, s45
	s_addc_u32 s25, s9, 0
	v_pk_fma_f16 v148, v65, v56, v148 op_sel:[0,0,0] op_sel_hi:[0,1,1] neg_lo:[0,0,1] neg_hi:[0,0,1]
	v_pk_fma_f16 v149, v65, v57, v149 op_sel:[0,0,0] op_sel_hi:[0,1,1] neg_lo:[0,0,1] neg_hi:[0,0,1]
	v_pk_fma_f16 v150, v65, v58, v150 op_sel:[0,0,0] op_sel_hi:[0,1,1] neg_lo:[0,0,1] neg_hi:[0,0,1]
	v_pk_fma_f16 v151, v65, v59, v151 op_sel:[0,0,0] op_sel_hi:[0,1,1] neg_lo:[0,0,1] neg_hi:[0,0,1]
	ds_read_b128 v[128:131], v161 offset:12288
	ds_read_b128 v[132:135], v161 offset:13312
	ds_read_b128 v[136:139], v161 offset:14336
	ds_read_b128 v[140:143], v161 offset:15360
	s_add_u32 s19, s19, 0x4000
	s_cmp_eq_u32 s19, 0x18000
	s_cselect_b32 s19, 0, s19
	v_add_u32_e32 v161, s19, v160
	s_waitcnt lgkmcnt(4)
	v_mfma_f32_32x32x16_f16 v[16:31], v[144:147], v[112:115], v[16:31]
	v_mfma_f32_32x32x16_f16 v[0:15], v[144:147], v[116:119], v[0:15]
	v_mfma_f32_32x32x16_f16 v[16:31], v[148:151], v[120:123], v[16:31]
	v_mfma_f32_32x32x16_f16 v[0:15], v[148:151], v[124:127], v[0:15]
	s_add_u32 s26, s24, 0x100000
	s_addc_u32 s27, s25, 0
	s_lshl_b32 s45, s43, 16
	s_add_u32 s28, s8, s45
	s_addc_u32 s29, s9, 0
	v_pk_mul_f16 v152, v73, v56 op_sel:[1,0] op_sel_hi:[1,1]
	v_pk_mul_f16 v153, v73, v57 op_sel:[1,0] op_sel_hi:[1,1]
	v_pk_mul_f16 v154, v73, v58 op_sel:[1,0] op_sel_hi:[1,1]
	v_pk_mul_f16 v155, v73, v59 op_sel:[1,0] op_sel_hi:[1,1]
	s_add_u32 s30, s28, 0x100000
	s_addc_u32 s31, s29, 0
	v_pk_fma_f16 v152, v65, v60, v152 op_sel:[1,0,0] op_sel_hi:[1,1,1]
	v_pk_fma_f16 v153, v65, v61, v153 op_sel:[1,0,0] op_sel_hi:[1,1,1]
	v_pk_fma_f16 v154, v65, v62, v154 op_sel:[1,0,0] op_sel_hi:[1,1,1]
	v_pk_fma_f16 v155, v65, v63, v155 op_sel:[1,0,0] op_sel_hi:[1,1,1]
	global_load_dwordx4 v[36:39], v164, s[24:25]
	v_pk_mul_f16 v156, v73, v60 op_sel:[1,0] op_sel_hi:[1,1]
	v_pk_mul_f16 v157, v73, v61 op_sel:[1,0] op_sel_hi:[1,1]
	v_pk_mul_f16 v158, v73, v62 op_sel:[1,0] op_sel_hi:[1,1]
	v_pk_mul_f16 v159, v73, v63 op_sel:[1,0] op_sel_hi:[1,1]
	global_load_dwordx4 v[32:35], v164, s[26:27]
	v_pk_fma_f16 v156, v65, v56, v156 op_sel:[1,0,0] op_sel_hi:[1,1,1] neg_lo:[0,0,1] neg_hi:[0,0,1]
	v_pk_fma_f16 v157, v65, v57, v157 op_sel:[1,0,0] op_sel_hi:[1,1,1] neg_lo:[0,0,1] neg_hi:[0,0,1]
	v_pk_fma_f16 v158, v65, v58, v158 op_sel:[1,0,0] op_sel_hi:[1,1,1] neg_lo:[0,0,1] neg_hi:[0,0,1]
	v_pk_fma_f16 v159, v65, v59, v159 op_sel:[1,0,0] op_sel_hi:[1,1,1] neg_lo:[0,0,1] neg_hi:[0,0,1]
	ds_read_b128 v[80:83], v161
	ds_read_b128 v[84:87], v161 offset:1024
	ds_read_b128 v[88:91], v161 offset:2048
	ds_read_b128 v[92:95], v161 offset:3072
	s_waitcnt lgkmcnt(4)
	v_mfma_f32_32x32x16_f16 v[16:31], v[152:155], v[128:131], v[16:31]
	v_mfma_f32_32x32x16_f16 v[0:15], v[152:155], v[132:135], v[0:15]
	v_mfma_f32_32x32x16_f16 v[16:31], v[156:159], v[136:139], v[16:31]
	v_mfma_f32_32x32x16_f16 v[0:15], v[156:159], v[140:143], v[0:15]
	global_load_dwordx4 v[40:43], v165, s[28:29]
	v_pk_mul_f16 v144, v74, v56 op_sel:[0,0] op_sel_hi:[0,1]
	v_pk_mul_f16 v145, v74, v57 op_sel:[0,0] op_sel_hi:[0,1]
	v_pk_mul_f16 v146, v74, v58 op_sel:[0,0] op_sel_hi:[0,1]
	v_pk_mul_f16 v147, v74, v59 op_sel:[0,0] op_sel_hi:[0,1]
	global_load_dwordx4 v[44:47], v166, s[28:29]
	v_pk_fma_f16 v144, v66, v60, v144 op_sel:[0,0,0] op_sel_hi:[0,1,1]
	v_pk_fma_f16 v145, v66, v61, v145 op_sel:[0,0,0] op_sel_hi:[0,1,1]
	v_pk_fma_f16 v146, v66, v62, v146 op_sel:[0,0,0] op_sel_hi:[0,1,1]
	v_pk_fma_f16 v147, v66, v63, v147 op_sel:[0,0,0] op_sel_hi:[0,1,1]
	global_load_dwordx4 v[48:51], v165, s[30:31]
	v_pk_mul_f16 v148, v74, v60 op_sel:[0,0] op_sel_hi:[0,1]
	v_pk_mul_f16 v149, v74, v61 op_sel:[0,0] op_sel_hi:[0,1]
	v_pk_mul_f16 v150, v74, v62 op_sel:[0,0] op_sel_hi:[0,1]
	v_pk_mul_f16 v151, v74, v63 op_sel:[0,0] op_sel_hi:[0,1]
	global_load_dwordx4 v[52:55], v166, s[30:31]
	v_pk_fma_f16 v148, v66, v56, v148 op_sel:[0,0,0] op_sel_hi:[0,1,1] neg_lo:[0,0,1] neg_hi:[0,0,1]
	v_pk_fma_f16 v149, v66, v57, v149 op_sel:[0,0,0] op_sel_hi:[0,1,1] neg_lo:[0,0,1] neg_hi:[0,0,1]
	v_pk_fma_f16 v150, v66, v58, v150 op_sel:[0,0,0] op_sel_hi:[0,1,1] neg_lo:[0,0,1] neg_hi:[0,0,1]
	v_pk_fma_f16 v151, v66, v59, v151 op_sel:[0,0,0] op_sel_hi:[0,1,1] neg_lo:[0,0,1] neg_hi:[0,0,1]
	ds_read_b128 v[96:99], v161 offset:4096
	ds_read_b128 v[100:103], v161 offset:5120
	ds_read_b128 v[104:107], v161 offset:6144
	ds_read_b128 v[108:111], v161 offset:7168
	s_add_u32 s17, s17, 1
	s_cmp_eq_u32 s17, 17
	s_cbranch_scc1 .Lk2_epi

.Lk2_b11:
	s_waitcnt lgkmcnt(4)
	v_mfma_f32_32x32x16_f16 v[16:31], v[144:147], v[80:83], v[16:31]
	v_mfma_f32_32x32x16_f16 v[0:15], v[144:147], v[84:87], v[0:15]
	v_mfma_f32_32x32x16_f16 v[16:31], v[148:151], v[88:91], v[16:31]
	v_mfma_f32_32x32x16_f16 v[0:15], v[148:151], v[92:95], v[0:15]
	s_cmp_le_u32 s22, 16
	s_cselect_b32 s40, s18, 0x18000
	s_add_u32 m0, s40, s35
	v_pk_mul_f16 v152, v74, v56 op_sel:[1,0] op_sel_hi:[1,1]
	v_pk_mul_f16 v153, v74, v57 op_sel:[1,0] op_sel_hi:[1,1]
	v_pk_mul_f16 v154, v74, v58 op_sel:[1,0] op_sel_hi:[1,1]
	v_pk_mul_f16 v155, v74, v59 op_sel:[1,0] op_sel_hi:[1,1]
	s_add_u32 s22, s22, 1
	global_load_lds_dwordx4 v168, s[20:21]
	global_load_lds_dwordx4 v168, s[20:21] offset:1024
	v_pk_fma_f16 v152, v66, v60, v152 op_sel:[1,0,0] op_sel_hi:[1,1,1]
	v_pk_fma_f16 v153, v66, v61, v153 op_sel:[1,0,0] op_sel_hi:[1,1,1]
	v_pk_fma_f16 v154, v66, v62, v154 op_sel:[1,0,0] op_sel_hi:[1,1,1]
	v_pk_fma_f16 v155, v66, v63, v155 op_sel:[1,0,0] op_sel_hi:[1,1,1]
	s_cmp_le_u32 s22, 16
	s_cselect_b32 s41, 0x4000, 0
	v_pk_mul_f16 v156, v74, v60 op_sel:[1,0] op_sel_hi:[1,1]
	v_pk_mul_f16 v157, v74, v61 op_sel:[1,0] op_sel_hi:[1,1]
	v_pk_mul_f16 v158, v74, v62 op_sel:[1,0] op_sel_hi:[1,1]
	v_pk_mul_f16 v159, v74, v63 op_sel:[1,0] op_sel_hi:[1,1]
	s_add_u32 s20, s20, s41
	s_addc_u32 s21, s21, 0
	v_pk_fma_f16 v156, v66, v56, v156 op_sel:[1,0,0] op_sel_hi:[1,1,1] neg_lo:[0,0,1] neg_hi:[0,0,1]
	v_pk_fma_f16 v157, v66, v57, v157 op_sel:[1,0,0] op_sel_hi:[1,1,1] neg_lo:[0,0,1] neg_hi:[0,0,1]
	v_pk_fma_f16 v158, v66, v58, v158 op_sel:[1,0,0] op_sel_hi:[1,1,1] neg_lo:[0,0,1] neg_hi:[0,0,1]
	v_pk_fma_f16 v159, v66, v59, v159 op_sel:[1,0,0] op_sel_hi:[1,1,1] neg_lo:[0,0,1] neg_hi:[0,0,1]
	ds_read_b128 v[112:115], v161 offset:8192
	ds_read_b128 v[116:119], v161 offset:9216
	ds_read_b128 v[120:123], v161 offset:10240
	ds_read_b128 v[124:127], v161 offset:11264
	s_waitcnt lgkmcnt(4)
	v_mfma_f32_32x32x16_f16 v[16:31], v[152:155], v[96:99], v[16:31]
	v_mfma_f32_32x32x16_f16 v[0:15], v[152:155], v[100:103], v[0:15]
	v_mfma_f32_32x32x16_f16 v[16:31], v[156:159], v[104:107], v[16:31]
	v_mfma_f32_32x32x16_f16 v[0:15], v[156:159], v[108:111], v[0:15]
	s_add_u32 s18, s18, 0x4000
	s_cmp_eq_u32 s18, 0x18000
	s_cselect_b32 s18, 0, s18
	v_pk_mul_f16 v144, v75, v56 op_sel:[0,0] op_sel_hi:[0,1]
	v_pk_mul_f16 v145, v75, v57 op_sel:[0,0] op_sel_hi:[0,1]
	v_pk_mul_f16 v146, v75, v58 op_sel:[0,0] op_sel_hi:[0,1]
	v_pk_mul_f16 v147, v75, v59 op_sel:[0,0] op_sel_hi:[0,1]
	v_pk_fma_f16 v144, v67, v60, v144 op_sel:[0,0,0] op_sel_hi:[0,1,1]
	v_pk_fma_f16 v145, v67, v61, v145 op_sel:[0,0,0] op_sel_hi:[0,1,1]
	v_pk_fma_f16 v146, v67, v62, v146 op_sel:[0,0,0] op_sel_hi:[0,1,1]
	v_pk_fma_f16 v147, v67, v63, v147 op_sel:[0,0,0] op_sel_hi:[0,1,1]
	v_pk_mul_f16 v148, v75, v60 op_sel:[0,0] op_sel_hi:[0,1]
	v_pk_mul_f16 v149, v75, v61 op_sel:[0,0] op_sel_hi:[0,1]
	v_pk_mul_f16 v150, v75, v62 op_sel:[0,0] op_sel_hi:[0,1]
	v_pk_mul_f16 v151, v75, v63 op_sel:[0,0] op_sel_hi:[0,1]
	v_pk_fma_f16 v148, v67, v56, v148 op_sel:[0,0,0] op_sel_hi:[0,1,1] neg_lo:[0,0,1] neg_hi:[0,0,1]
	v_pk_fma_f16 v149, v67, v57, v149 op_sel:[0,0,0] op_sel_hi:[0,1,1] neg_lo:[0,0,1] neg_hi:[0,0,1]
	v_pk_fma_f16 v150, v67, v58, v150 op_sel:[0,0,0] op_sel_hi:[0,1,1] neg_lo:[0,0,1] neg_hi:[0,0,1]
	v_pk_fma_f16 v151, v67, v59, v151 op_sel:[0,0,0] op_sel_hi:[0,1,1] neg_lo:[0,0,1] neg_hi:[0,0,1]
	ds_read_b128 v[128:131], v161 offset:12288
	ds_read_b128 v[132:135], v161 offset:13312
	ds_read_b128 v[136:139], v161 offset:14336
	ds_read_b128 v[140:143], v161 offset:15360
	s_add_u32 s19, s19, 0x4000
	s_cmp_eq_u32 s19, 0x18000
	s_cselect_b32 s19, 0, s19
	v_add_u32_e32 v161, s19, v160
	s_waitcnt lgkmcnt(4)
	v_mfma_f32_32x32x16_f16 v[16:31], v[144:147], v[112:115], v[16:31]
	v_mfma_f32_32x32x16_f16 v[0:15], v[144:147], v[116:119], v[0:15]
	v_mfma_f32_32x32x16_f16 v[16:31], v[148:151], v[120:123], v[16:31]
	v_mfma_f32_32x32x16_f16 v[0:15], v[148:151], v[124:127], v[0:15]
	v_pk_mul_f16 v152, v75, v56 op_sel:[1,0] op_sel_hi:[1,1]
	v_pk_mul_f16 v153, v75, v57 op_sel:[1,0] op_sel_hi:[1,1]
	v_pk_mul_f16 v154, v75, v58 op_sel:[1,0] op_sel_hi:[1,1]
	v_pk_mul_f16 v155, v75, v59 op_sel:[1,0] op_sel_hi:[1,1]
	v_pk_fma_f16 v152, v67, v60, v152 op_sel:[1,0,0] op_sel_hi:[1,1,1]
	v_pk_fma_f16 v153, v67, v61, v153 op_sel:[1,0,0] op_sel_hi:[1,1,1]
	v_pk_fma_f16 v154, v67, v62, v154 op_sel:[1,0,0] op_sel_hi:[1,1,1]
	v_pk_fma_f16 v155, v67, v63, v155 op_sel:[1,0,0] op_sel_hi:[1,1,1]
	v_pk_mul_f16 v156, v75, v60 op_sel:[1,0] op_sel_hi:[1,1]
	v_pk_mul_f16 v157, v75, v61 op_sel:[1,0] op_sel_hi:[1,1]
	v_pk_mul_f16 v158, v75, v62 op_sel:[1,0] op_sel_hi:[1,1]
	v_pk_mul_f16 v159, v75, v63 op_sel:[1,0] op_sel_hi:[1,1]
	v_pk_fma_f16 v156, v67, v56, v156 op_sel:[1,0,0] op_sel_hi:[1,1,1] neg_lo:[0,0,1] neg_hi:[0,0,1]
	v_pk_fma_f16 v157, v67, v57, v157 op_sel:[1,0,0] op_sel_hi:[1,1,1] neg_lo:[0,0,1] neg_hi:[0,0,1]
	v_pk_fma_f16 v158, v67, v58, v158 op_sel:[1,0,0] op_sel_hi:[1,1,1] neg_lo:[0,0,1] neg_hi:[0,0,1]
	v_pk_fma_f16 v159, v67, v59, v159 op_sel:[1,0,0] op_sel_hi:[1,1,1] neg_lo:[0,0,1] neg_hi:[0,0,1]
	ds_read_b128 v[80:83], v161
	ds_read_b128 v[84:87], v161 offset:1024
	ds_read_b128 v[88:91], v161 offset:2048
	ds_read_b128 v[92:95], v161 offset:3072
	s_waitcnt lgkmcnt(4)
	v_mfma_f32_32x32x16_f16 v[16:31], v[152:155], v[128:131], v[16:31]
	v_mfma_f32_32x32x16_f16 v[0:15], v[152:155], v[132:135], v[0:15]
	v_mfma_f32_32x32x16_f16 v[16:31], v[156:159], v[136:139], v[16:31]
	v_mfma_f32_32x32x16_f16 v[0:15], v[156:159], v[140:143], v[0:15]
	v_pk_mul_f16 v144, v76, v56 op_sel:[0,0] op_sel_hi:[0,1]
	v_pk_mul_f16 v145, v76, v57 op_sel:[0,0] op_sel_hi:[0,1]
	v_pk_mul_f16 v146, v76, v58 op_sel:[0,0] op_sel_hi:[0,1]
	v_pk_mul_f16 v147, v76, v59 op_sel:[0,0] op_sel_hi:[0,1]
	v_pk_fma_f16 v144, v68, v60, v144 op_sel:[0,0,0] op_sel_hi:[0,1,1]
	v_pk_fma_f16 v145, v68, v61, v145 op_sel:[0,0,0] op_sel_hi:[0,1,1]
	v_pk_fma_f16 v146, v68, v62, v146 op_sel:[0,0,0] op_sel_hi:[0,1,1]
	v_pk_fma_f16 v147, v68, v63, v147 op_sel:[0,0,0] op_sel_hi:[0,1,1]
	v_pk_mul_f16 v148, v76, v60 op_sel:[0,0] op_sel_hi:[0,1]
	v_pk_mul_f16 v149, v76, v61 op_sel:[0,0] op_sel_hi:[0,1]
	v_pk_mul_f16 v150, v76, v62 op_sel:[0,0] op_sel_hi:[0,1]
	v_pk_mul_f16 v151, v76, v63 op_sel:[0,0] op_sel_hi:[0,1]
	v_pk_fma_f16 v148, v68, v56, v148 op_sel:[0,0,0] op_sel_hi:[0,1,1] neg_lo:[0,0,1] neg_hi:[0,0,1]
	v_pk_fma_f16 v149, v68, v57, v149 op_sel:[0,0,0] op_sel_hi:[0,1,1] neg_lo:[0,0,1] neg_hi:[0,0,1]
	v_pk_fma_f16 v150, v68, v58, v150 op_sel:[0,0,0] op_sel_hi:[0,1,1] neg_lo:[0,0,1] neg_hi:[0,0,1]
	v_pk_fma_f16 v151, v68, v59, v151 op_sel:[0,0,0] op_sel_hi:[0,1,1] neg_lo:[0,0,1] neg_hi:[0,0,1]
	ds_read_b128 v[96:99], v161 offset:4096
	ds_read_b128 v[100:103], v161 offset:5120
	ds_read_b128 v[104:107], v161 offset:6144
	ds_read_b128 v[108:111], v161 offset:7168
	s_add_u32 s17, s17, 1
	s_cmp_eq_u32 s17, 17
	s_cbranch_scc1 .Lk2_epi

.Lk2_b12:
	s_waitcnt lgkmcnt(4)
	v_mfma_f32_32x32x16_f16 v[16:31], v[144:147], v[80:83], v[16:31]
	v_mfma_f32_32x32x16_f16 v[0:15], v[144:147], v[84:87], v[0:15]
	v_mfma_f32_32x32x16_f16 v[16:31], v[148:151], v[88:91], v[16:31]
	v_mfma_f32_32x32x16_f16 v[0:15], v[148:151], v[92:95], v[0:15]
	s_cmp_le_u32 s22, 16
	s_cselect_b32 s40, s18, 0x18000
	s_add_u32 m0, s40, s35
	v_pk_mul_f16 v152, v76, v56 op_sel:[1,0] op_sel_hi:[1,1]
	v_pk_mul_f16 v153, v76, v57 op_sel:[1,0] op_sel_hi:[1,1]
	v_pk_mul_f16 v154, v76, v58 op_sel:[1,0] op_sel_hi:[1,1]
	v_pk_mul_f16 v155, v76, v59 op_sel:[1,0] op_sel_hi:[1,1]
	s_add_u32 s22, s22, 1
	global_load_lds_dwordx4 v168, s[20:21]
	global_load_lds_dwordx4 v168, s[20:21] offset:1024
	v_pk_fma_f16 v152, v68, v60, v152 op_sel:[1,0,0] op_sel_hi:[1,1,1]
	v_pk_fma_f16 v153, v68, v61, v153 op_sel:[1,0,0] op_sel_hi:[1,1,1]
	v_pk_fma_f16 v154, v68, v62, v154 op_sel:[1,0,0] op_sel_hi:[1,1,1]
	v_pk_fma_f16 v155, v68, v63, v155 op_sel:[1,0,0] op_sel_hi:[1,1,1]
	s_cmp_le_u32 s22, 16
	s_cselect_b32 s41, 0x4000, 0
	v_pk_mul_f16 v156, v76, v60 op_sel:[1,0] op_sel_hi:[1,1]
	v_pk_mul_f16 v157, v76, v61 op_sel:[1,0] op_sel_hi:[1,1]
	v_pk_mul_f16 v158, v76, v62 op_sel:[1,0] op_sel_hi:[1,1]
	v_pk_mul_f16 v159, v76, v63 op_sel:[1,0] op_sel_hi:[1,1]
	s_add_u32 s20, s20, s41
	s_addc_u32 s21, s21, 0
	v_pk_fma_f16 v156, v68, v56, v156 op_sel:[1,0,0] op_sel_hi:[1,1,1] neg_lo:[0,0,1] neg_hi:[0,0,1]
	v_pk_fma_f16 v157, v68, v57, v157 op_sel:[1,0,0] op_sel_hi:[1,1,1] neg_lo:[0,0,1] neg_hi:[0,0,1]
	v_pk_fma_f16 v158, v68, v58, v158 op_sel:[1,0,0] op_sel_hi:[1,1,1] neg_lo:[0,0,1] neg_hi:[0,0,1]
	v_pk_fma_f16 v159, v68, v59, v159 op_sel:[1,0,0] op_sel_hi:[1,1,1] neg_lo:[0,0,1] neg_hi:[0,0,1]
	ds_read_b128 v[112:115], v161 offset:8192
	ds_read_b128 v[116:119], v161 offset:9216
	ds_read_b128 v[120:123], v161 offset:10240
	ds_read_b128 v[124:127], v161 offset:11264
	s_waitcnt lgkmcnt(4)
	v_mfma_f32_32x32x16_f16 v[16:31], v[152:155], v[96:99], v[16:31]
	v_mfma_f32_32x32x16_f16 v[0:15], v[152:155], v[100:103], v[0:15]
	v_mfma_f32_32x32x16_f16 v[16:31], v[156:159], v[104:107], v[16:31]
	v_mfma_f32_32x32x16_f16 v[0:15], v[156:159], v[108:111], v[0:15]
	s_add_u32 s18, s18, 0x4000
	s_cmp_eq_u32 s18, 0x18000
	s_cselect_b32 s18, 0, s18
	v_pk_mul_f16 v144, v77, v56 op_sel:[0,0] op_sel_hi:[0,1]
	v_pk_mul_f16 v145, v77, v57 op_sel:[0,0] op_sel_hi:[0,1]
	v_pk_mul_f16 v146, v77, v58 op_sel:[0,0] op_sel_hi:[0,1]
	v_pk_mul_f16 v147, v77, v59 op_sel:[0,0] op_sel_hi:[0,1]
	v_pk_fma_f16 v144, v69, v60, v144 op_sel:[0,0,0] op_sel_hi:[0,1,1]
	v_pk_fma_f16 v145, v69, v61, v145 op_sel:[0,0,0] op_sel_hi:[0,1,1]
	v_pk_fma_f16 v146, v69, v62, v146 op_sel:[0,0,0] op_sel_hi:[0,1,1]
	v_pk_fma_f16 v147, v69, v63, v147 op_sel:[0,0,0] op_sel_hi:[0,1,1]
	v_pk_mul_f16 v148, v77, v60 op_sel:[0,0] op_sel_hi:[0,1]
	v_pk_mul_f16 v149, v77, v61 op_sel:[0,0] op_sel_hi:[0,1]
	v_pk_mul_f16 v150, v77, v62 op_sel:[0,0] op_sel_hi:[0,1]
	v_pk_mul_f16 v151, v77, v63 op_sel:[0,0] op_sel_hi:[0,1]
	v_pk_fma_f16 v148, v69, v56, v148 op_sel:[0,0,0] op_sel_hi:[0,1,1] neg_lo:[0,0,1] neg_hi:[0,0,1]
	v_pk_fma_f16 v149, v69, v57, v149 op_sel:[0,0,0] op_sel_hi:[0,1,1] neg_lo:[0,0,1] neg_hi:[0,0,1]
	v_pk_fma_f16 v150, v69, v58, v150 op_sel:[0,0,0] op_sel_hi:[0,1,1] neg_lo:[0,0,1] neg_hi:[0,0,1]
	v_pk_fma_f16 v151, v69, v59, v151 op_sel:[0,0,0] op_sel_hi:[0,1,1] neg_lo:[0,0,1] neg_hi:[0,0,1]
	ds_read_b128 v[128:131], v161 offset:12288
	ds_read_b128 v[132:135], v161 offset:13312
	ds_read_b128 v[136:139], v161 offset:14336
	ds_read_b128 v[140:143], v161 offset:15360
	s_add_u32 s19, s19, 0x4000
	s_cmp_eq_u32 s19, 0x18000
	s_cselect_b32 s19, 0, s19
	v_add_u32_e32 v161, s19, v160
	s_waitcnt lgkmcnt(4)
	v_mfma_f32_32x32x16_f16 v[16:31], v[144:147], v[112:115], v[16:31]
	v_mfma_f32_32x32x16_f16 v[0:15], v[144:147], v[116:119], v[0:15]
	v_mfma_f32_32x32x16_f16 v[16:31], v[148:151], v[120:123], v[16:31]
	v_mfma_f32_32x32x16_f16 v[0:15], v[148:151], v[124:127], v[0:15]
	v_pk_mul_f16 v152, v77, v56 op_sel:[1,0] op_sel_hi:[1,1]
	v_pk_mul_f16 v153, v77, v57 op_sel:[1,0] op_sel_hi:[1,1]
	v_pk_mul_f16 v154, v77, v58 op_sel:[1,0] op_sel_hi:[1,1]
	v_pk_mul_f16 v155, v77, v59 op_sel:[1,0] op_sel_hi:[1,1]
	v_pk_fma_f16 v152, v69, v60, v152 op_sel:[1,0,0] op_sel_hi:[1,1,1]
	v_pk_fma_f16 v153, v69, v61, v153 op_sel:[1,0,0] op_sel_hi:[1,1,1]
	v_pk_fma_f16 v154, v69, v62, v154 op_sel:[1,0,0] op_sel_hi:[1,1,1]
	v_pk_fma_f16 v155, v69, v63, v155 op_sel:[1,0,0] op_sel_hi:[1,1,1]
	v_pk_mul_f16 v156, v77, v60 op_sel:[1,0] op_sel_hi:[1,1]
	v_pk_mul_f16 v157, v77, v61 op_sel:[1,0] op_sel_hi:[1,1]
	v_pk_mul_f16 v158, v77, v62 op_sel:[1,0] op_sel_hi:[1,1]
	v_pk_mul_f16 v159, v77, v63 op_sel:[1,0] op_sel_hi:[1,1]
	v_pk_fma_f16 v156, v69, v56, v156 op_sel:[1,0,0] op_sel_hi:[1,1,1] neg_lo:[0,0,1] neg_hi:[0,0,1]
	v_pk_fma_f16 v157, v69, v57, v157 op_sel:[1,0,0] op_sel_hi:[1,1,1] neg_lo:[0,0,1] neg_hi:[0,0,1]
	v_pk_fma_f16 v158, v69, v58, v158 op_sel:[1,0,0] op_sel_hi:[1,1,1] neg_lo:[0,0,1] neg_hi:[0,0,1]
	v_pk_fma_f16 v159, v69, v59, v159 op_sel:[1,0,0] op_sel_hi:[1,1,1] neg_lo:[0,0,1] neg_hi:[0,0,1]
	ds_read_b128 v[80:83], v161
	ds_read_b128 v[84:87], v161 offset:1024
	ds_read_b128 v[88:91], v161 offset:2048
	ds_read_b128 v[92:95], v161 offset:3072
	s_waitcnt lgkmcnt(4)
	v_mfma_f32_32x32x16_f16 v[16:31], v[152:155], v[128:131], v[16:31]
	v_mfma_f32_32x32x16_f16 v[0:15], v[152:155], v[132:135], v[0:15]
	v_mfma_f32_32x32x16_f16 v[16:31], v[156:159], v[136:139], v[16:31]
	v_mfma_f32_32x32x16_f16 v[0:15], v[156:159], v[140:143], v[0:15]
	v_pk_mul_f16 v144, v78, v56 op_sel:[0,0] op_sel_hi:[0,1]
	v_pk_mul_f16 v145, v78, v57 op_sel:[0,0] op_sel_hi:[0,1]
	v_pk_mul_f16 v146, v78, v58 op_sel:[0,0] op_sel_hi:[0,1]
	v_pk_mul_f16 v147, v78, v59 op_sel:[0,0] op_sel_hi:[0,1]
	v_pk_fma_f16 v144, v70, v60, v144 op_sel:[0,0,0] op_sel_hi:[0,1,1]
	v_pk_fma_f16 v145, v70, v61, v145 op_sel:[0,0,0] op_sel_hi:[0,1,1]
	v_pk_fma_f16 v146, v70, v62, v146 op_sel:[0,0,0] op_sel_hi:[0,1,1]
	v_pk_fma_f16 v147, v70, v63, v147 op_sel:[0,0,0] op_sel_hi:[0,1,1]
	v_pk_mul_f16 v148, v78, v60 op_sel:[0,0] op_sel_hi:[0,1]
	v_pk_mul_f16 v149, v78, v61 op_sel:[0,0] op_sel_hi:[0,1]
	v_pk_mul_f16 v150, v78, v62 op_sel:[0,0] op_sel_hi:[0,1]
	v_pk_mul_f16 v151, v78, v63 op_sel:[0,0] op_sel_hi:[0,1]
	v_pk_fma_f16 v148, v70, v56, v148 op_sel:[0,0,0] op_sel_hi:[0,1,1] neg_lo:[0,0,1] neg_hi:[0,0,1]
	v_pk_fma_f16 v149, v70, v57, v149 op_sel:[0,0,0] op_sel_hi:[0,1,1] neg_lo:[0,0,1] neg_hi:[0,0,1]
	v_pk_fma_f16 v150, v70, v58, v150 op_sel:[0,0,0] op_sel_hi:[0,1,1] neg_lo:[0,0,1] neg_hi:[0,0,1]
	v_pk_fma_f16 v151, v70, v59, v151 op_sel:[0,0,0] op_sel_hi:[0,1,1] neg_lo:[0,0,1] neg_hi:[0,0,1]
	ds_read_b128 v[96:99], v161 offset:4096
	ds_read_b128 v[100:103], v161 offset:5120
	ds_read_b128 v[104:107], v161 offset:6144
	ds_read_b128 v[108:111], v161 offset:7168
	s_add_u32 s17, s17, 1
	s_cmp_eq_u32 s17, 17
	s_cbranch_scc1 .Lk2_epi

.Lk2_b13:
	s_waitcnt lgkmcnt(4)
	v_mfma_f32_32x32x16_f16 v[16:31], v[144:147], v[80:83], v[16:31]
	v_mfma_f32_32x32x16_f16 v[0:15], v[144:147], v[84:87], v[0:15]
	v_mfma_f32_32x32x16_f16 v[16:31], v[148:151], v[88:91], v[16:31]
	v_mfma_f32_32x32x16_f16 v[0:15], v[148:151], v[92:95], v[0:15]
	s_cmp_le_u32 s22, 16
	s_cselect_b32 s40, s18, 0x18000
	s_add_u32 m0, s40, s35
	v_pk_mul_f16 v152, v78, v56 op_sel:[1,0] op_sel_hi:[1,1]
	v_pk_mul_f16 v153, v78, v57 op_sel:[1,0] op_sel_hi:[1,1]
	v_pk_mul_f16 v154, v78, v58 op_sel:[1,0] op_sel_hi:[1,1]
	v_pk_mul_f16 v155, v78, v59 op_sel:[1,0] op_sel_hi:[1,1]
	s_add_u32 s22, s22, 1
	global_load_lds_dwordx4 v168, s[20:21]
	global_load_lds_dwordx4 v168, s[20:21] offset:1024
	v_pk_fma_f16 v152, v70, v60, v152 op_sel:[1,0,0] op_sel_hi:[1,1,1]
	v_pk_fma_f16 v153, v70, v61, v153 op_sel:[1,0,0] op_sel_hi:[1,1,1]
	v_pk_fma_f16 v154, v70, v62, v154 op_sel:[1,0,0] op_sel_hi:[1,1,1]
	v_pk_fma_f16 v155, v70, v63, v155 op_sel:[1,0,0] op_sel_hi:[1,1,1]
	s_cmp_le_u32 s22, 16
	s_cselect_b32 s41, 0x4000, 0
	v_pk_mul_f16 v156, v78, v60 op_sel:[1,0] op_sel_hi:[1,1]
	v_pk_mul_f16 v157, v78, v61 op_sel:[1,0] op_sel_hi:[1,1]
	v_pk_mul_f16 v158, v78, v62 op_sel:[1,0] op_sel_hi:[1,1]
	v_pk_mul_f16 v159, v78, v63 op_sel:[1,0] op_sel_hi:[1,1]
	s_add_u32 s20, s20, s41
	s_addc_u32 s21, s21, 0
	v_pk_fma_f16 v156, v70, v56, v156 op_sel:[1,0,0] op_sel_hi:[1,1,1] neg_lo:[0,0,1] neg_hi:[0,0,1]
	v_pk_fma_f16 v157, v70, v57, v157 op_sel:[1,0,0] op_sel_hi:[1,1,1] neg_lo:[0,0,1] neg_hi:[0,0,1]
	v_pk_fma_f16 v158, v70, v58, v158 op_sel:[1,0,0] op_sel_hi:[1,1,1] neg_lo:[0,0,1] neg_hi:[0,0,1]
	v_pk_fma_f16 v159, v70, v59, v159 op_sel:[1,0,0] op_sel_hi:[1,1,1] neg_lo:[0,0,1] neg_hi:[0,0,1]
	ds_read_b128 v[112:115], v161 offset:8192
	ds_read_b128 v[116:119], v161 offset:9216
	ds_read_b128 v[120:123], v161 offset:10240
	ds_read_b128 v[124:127], v161 offset:11264
	s_waitcnt lgkmcnt(4)
	v_mfma_f32_32x32x16_f16 v[16:31], v[152:155], v[96:99], v[16:31]
	v_mfma_f32_32x32x16_f16 v[0:15], v[152:155], v[100:103], v[0:15]
	v_mfma_f32_32x32x16_f16 v[16:31], v[156:159], v[104:107], v[16:31]
	v_mfma_f32_32x32x16_f16 v[0:15], v[156:159], v[108:111], v[0:15]
	s_add_u32 s18, s18, 0x4000
	s_cmp_eq_u32 s18, 0x18000
	s_cselect_b32 s18, 0, s18
	v_pk_mul_f16 v144, v79, v56 op_sel:[0,0] op_sel_hi:[0,1]
	v_pk_mul_f16 v145, v79, v57 op_sel:[0,0] op_sel_hi:[0,1]
	v_pk_mul_f16 v146, v79, v58 op_sel:[0,0] op_sel_hi:[0,1]
	v_pk_mul_f16 v147, v79, v59 op_sel:[0,0] op_sel_hi:[0,1]
	v_pk_fma_f16 v144, v71, v60, v144 op_sel:[0,0,0] op_sel_hi:[0,1,1]
	v_pk_fma_f16 v145, v71, v61, v145 op_sel:[0,0,0] op_sel_hi:[0,1,1]
	v_pk_fma_f16 v146, v71, v62, v146 op_sel:[0,0,0] op_sel_hi:[0,1,1]
	v_pk_fma_f16 v147, v71, v63, v147 op_sel:[0,0,0] op_sel_hi:[0,1,1]
	v_pk_mul_f16 v148, v79, v60 op_sel:[0,0] op_sel_hi:[0,1]
	v_pk_mul_f16 v149, v79, v61 op_sel:[0,0] op_sel_hi:[0,1]
	v_pk_mul_f16 v150, v79, v62 op_sel:[0,0] op_sel_hi:[0,1]
	v_pk_mul_f16 v151, v79, v63 op_sel:[0,0] op_sel_hi:[0,1]
	v_pk_fma_f16 v148, v71, v56, v148 op_sel:[0,0,0] op_sel_hi:[0,1,1] neg_lo:[0,0,1] neg_hi:[0,0,1]
	v_pk_fma_f16 v149, v71, v57, v149 op_sel:[0,0,0] op_sel_hi:[0,1,1] neg_lo:[0,0,1] neg_hi:[0,0,1]
	v_pk_fma_f16 v150, v71, v58, v150 op_sel:[0,0,0] op_sel_hi:[0,1,1] neg_lo:[0,0,1] neg_hi:[0,0,1]
	v_pk_fma_f16 v151, v71, v59, v151 op_sel:[0,0,0] op_sel_hi:[0,1,1] neg_lo:[0,0,1] neg_hi:[0,0,1]
	ds_read_b128 v[128:131], v161 offset:12288
	ds_read_b128 v[132:135], v161 offset:13312
	ds_read_b128 v[136:139], v161 offset:14336
	ds_read_b128 v[140:143], v161 offset:15360
	s_add_u32 s19, s19, 0x4000
	s_cmp_eq_u32 s19, 0x18000
	s_cselect_b32 s19, 0, s19
	v_add_u32_e32 v161, s19, v160
	s_waitcnt lgkmcnt(4)
	v_mfma_f32_32x32x16_f16 v[16:31], v[144:147], v[112:115], v[16:31]
	v_mfma_f32_32x32x16_f16 v[0:15], v[144:147], v[116:119], v[0:15]
	v_mfma_f32_32x32x16_f16 v[16:31], v[148:151], v[120:123], v[16:31]
	v_mfma_f32_32x32x16_f16 v[0:15], v[148:151], v[124:127], v[0:15]
	v_pk_mul_f16 v152, v79, v56 op_sel:[1,0] op_sel_hi:[1,1]
	v_pk_mul_f16 v153, v79, v57 op_sel:[1,0] op_sel_hi:[1,1]
	v_pk_mul_f16 v154, v79, v58 op_sel:[1,0] op_sel_hi:[1,1]
	v_pk_mul_f16 v155, v79, v59 op_sel:[1,0] op_sel_hi:[1,1]
	v_pk_fma_f16 v152, v71, v60, v152 op_sel:[1,0,0] op_sel_hi:[1,1,1]
	v_pk_fma_f16 v153, v71, v61, v153 op_sel:[1,0,0] op_sel_hi:[1,1,1]
	v_pk_fma_f16 v154, v71, v62, v154 op_sel:[1,0,0] op_sel_hi:[1,1,1]
	v_pk_fma_f16 v155, v71, v63, v155 op_sel:[1,0,0] op_sel_hi:[1,1,1]
	v_pk_mul_f16 v156, v79, v60 op_sel:[1,0] op_sel_hi:[1,1]
	v_pk_mul_f16 v157, v79, v61 op_sel:[1,0] op_sel_hi:[1,1]
	v_pk_mul_f16 v158, v79, v62 op_sel:[1,0] op_sel_hi:[1,1]
	v_pk_mul_f16 v159, v79, v63 op_sel:[1,0] op_sel_hi:[1,1]
	v_pk_fma_f16 v156, v71, v56, v156 op_sel:[1,0,0] op_sel_hi:[1,1,1] neg_lo:[0,0,1] neg_hi:[0,0,1]
	v_pk_fma_f16 v157, v71, v57, v157 op_sel:[1,0,0] op_sel_hi:[1,1,1] neg_lo:[0,0,1] neg_hi:[0,0,1]
	v_pk_fma_f16 v158, v71, v58, v158 op_sel:[1,0,0] op_sel_hi:[1,1,1] neg_lo:[0,0,1] neg_hi:[0,0,1]
	v_pk_fma_f16 v159, v71, v59, v159 op_sel:[1,0,0] op_sel_hi:[1,1,1] neg_lo:[0,0,1] neg_hi:[0,0,1]
	ds_read_b128 v[80:83], v161
	ds_read_b128 v[84:87], v161 offset:1024
	ds_read_b128 v[88:91], v161 offset:2048
	ds_read_b128 v[92:95], v161 offset:3072
	s_waitcnt lgkmcnt(4)
	v_mfma_f32_32x32x16_f16 v[16:31], v[152:155], v[128:131], v[16:31]
	v_mfma_f32_32x32x16_f16 v[0:15], v[152:155], v[132:135], v[0:15]
	v_mfma_f32_32x32x16_f16 v[16:31], v[156:159], v[136:139], v[16:31]
	v_mfma_f32_32x32x16_f16 v[0:15], v[156:159], v[140:143], v[0:15]
	s_waitcnt vmcnt(6)
	v_pk_mul_f16 v144, v48, v32 op_sel:[0,0] op_sel_hi:[0,1]
	v_pk_mul_f16 v145, v48, v33 op_sel:[0,0] op_sel_hi:[0,1]
	v_pk_mul_f16 v146, v48, v34 op_sel:[0,0] op_sel_hi:[0,1]
	v_pk_mul_f16 v147, v48, v35 op_sel:[0,0] op_sel_hi:[0,1]
	v_pk_fma_f16 v144, v40, v36, v144 op_sel:[0,0,0] op_sel_hi:[0,1,1]
	v_pk_fma_f16 v145, v40, v37, v145 op_sel:[0,0,0] op_sel_hi:[0,1,1]
	v_pk_fma_f16 v146, v40, v38, v146 op_sel:[0,0,0] op_sel_hi:[0,1,1]
	v_pk_fma_f16 v147, v40, v39, v147 op_sel:[0,0,0] op_sel_hi:[0,1,1]
	v_pk_mul_f16 v148, v48, v36 op_sel:[0,0] op_sel_hi:[0,1]
	v_pk_mul_f16 v149, v48, v37 op_sel:[0,0] op_sel_hi:[0,1]
	v_pk_mul_f16 v150, v48, v38 op_sel:[0,0] op_sel_hi:[0,1]
	v_pk_mul_f16 v151, v48, v39 op_sel:[0,0] op_sel_hi:[0,1]
	v_pk_fma_f16 v148, v40, v32, v148 op_sel:[0,0,0] op_sel_hi:[0,1,1] neg_lo:[0,0,1] neg_hi:[0,0,1]
	v_pk_fma_f16 v149, v40, v33, v149 op_sel:[0,0,0] op_sel_hi:[0,1,1] neg_lo:[0,0,1] neg_hi:[0,0,1]
	v_pk_fma_f16 v150, v40, v34, v150 op_sel:[0,0,0] op_sel_hi:[0,1,1] neg_lo:[0,0,1] neg_hi:[0,0,1]
	v_pk_fma_f16 v151, v40, v35, v151 op_sel:[0,0,0] op_sel_hi:[0,1,1] neg_lo:[0,0,1] neg_hi:[0,0,1]
	ds_read_b128 v[96:99], v161 offset:4096
	ds_read_b128 v[100:103], v161 offset:5120
	ds_read_b128 v[104:107], v161 offset:6144
	ds_read_b128 v[108:111], v161 offset:7168
	s_add_u32 s17, s17, 1
	s_cmp_eq_u32 s17, 17
	s_cbranch_scc1 .Lk2_epi
	s_branch .Lk2_s00
